# grid barrier: release all workgroups from the TOP counter (drops TOPGEN and XGEN hops), on top of v74
# baseline (speedup 1.0000x reference)
; #define LAS __attribute__((address_space(3)))
; __global__ void __launch_bounds__(NWAVES * 64, 2) trunk_fwd(Args a) {
;     extern __shared__ __attribute__((aligned(16))) unsigned char lds_raw[];
;     LAS unsigned char* lds = (LAS unsigned char*)lds_raw;
;     volatile LAS unsigned* MISC = (volatile LAS unsigned*)(lds + MISC_OFF);
;     const int G = gridDim.x; const int bx = blockIdx.x; const int vcu = (G % 8 == 0) ? (bx % 8) * (G / 8) + bx / 8 : bx;
;     const int NGW = G * NWAVES;
;     gu32* ctl = (gu32*)(a.ws + WS_CTL);
;     const int wave0 = __builtin_amdgcn_readfirstlane((int)threadIdx.x >> 6);
;     for (int u = (int)__builtin_amdgcn_mbcnt_hi(~0u, __builtin_amdgcn_mbcnt_lo(~0u, 0u)) + 64 * wave0; u < (LDS_BYTES - LDSCTL_OFF) / 4; u += NWAVES * 64) ((LAS unsigned*)(lds + LDSCTL_OFF))[u] = 0u;
_Z9trunk_fwd4Args:
	s_mov_b32 s98, 0
	s_load_dword s85, s[0:1], 0xb0
	s_mov_b64 s[96:97], s[0:1]
	s_add_u32 s0, s96, 0xb0
	s_addc_u32 s1, s97, 0
	s_mov_b32 s84, s2
	v_writelane_b32 v251, s0, 0
	s_nop 1
	v_writelane_b32 v251, s1, 1
	s_waitcnt lgkmcnt(0)
	s_and_b32 s0, s85, 7
	s_cmp_lg_u32 s0, 0
	v_writelane_b32 v251, s84, 2
	s_cbranch_scc1 .LBB0_2
	s_ashr_i32 s1, s84, 31
	s_lshr_b32 s1, s1, 29
	s_add_i32 s1, s84, s1
	s_and_b32 s2, s1, -8
	s_ashr_i32 s0, s85, 3
	s_sub_i32 s2, s84, s2
	s_mul_i32 s0, s0, s2
	s_ashr_i32 s1, s1, 3
	s_add_i32 s0, s0, s1
	v_writelane_b32 v251, s0, 2

; __device__ __forceinline__ unsigned xb_ld(unsigned* p)              { return __hip_atomic_load(p, __ATOMIC_RELAXED, __HIP_MEMORY_SCOPE_AGENT); }
; __device__ __forceinline__ unsigned xb_add(unsigned* p, unsigned v) { return __hip_atomic_fetch_add(p, v, __ATOMIC_RELAXED, __HIP_MEMORY_SCOPE_AGENT); }
; #define XB_SPIN(cond, bar) do { unsigned _sp = 0; while (cond) { __builtin_amdgcn_s_sleep(1); \
;     if ((++_sp & 255u) == 0u) { if (xb_ld(&(bar)[XB_TMO])) break; if (_sp > XB_SPIN_CAP) { atomicAdd(&(bar)[XB_TMO], 1u); break; } } } } while (0)
; #define XB_TID() ((int)__builtin_amdgcn_mbcnt_hi(~0u, __builtin_amdgcn_mbcnt_lo(~0u, 0u)) + 64 * xb_wave_id)
; __device__ __forceinline__ void xcd_barrier(const XcdBarrier& b, const int xb_wave_id) {
;     asm volatile("s_waitcnt vmcnt(0)" ::: "memory");
;     __syncthreads();
;     if (XB_TID() == 0) {
;         unsigned* bar = b.bar;
;         __builtin_amdgcn_s_waitcnt(0);
;         unsigned nloc = b.st[0], nx = b.st[1];
;         if (nloc == 0u) { xcd_barrier_complete(bar, b.x, nloc, nx); b.st[0] = nloc; b.st[1] = nx; }
;         const unsigned old = xb_add(&bar[XB_XSUB(b.x)], 1u);
;         const unsigned gen = old / nloc;
;         if (old + 1u == (gen + 1u) * nloc) {
;             __builtin_amdgcn_fence(__ATOMIC_RELEASE, "agent");
;             asm volatile("s_waitcnt vmcnt(0)" ::: "memory");
;             const unsigned og = xb_add(&bar[XB_TOP], 1u);
;             const unsigned tg = og / nx;
;             if (og + 1u == (tg + 1u) * nx) xb_add(&bar[XB_TOPGEN], 1u);
;             else XB_SPIN(xb_ld(&bar[XB_TOPGEN]) == tg, bar);
;             __builtin_amdgcn_fence(__ATOMIC_ACQUIRE, "agent");
;             xb_add(&bar[XB_XGEN(b.x)], 1u);
;             asm volatile("s_waitcnt vmcnt(0)" ::: "memory");
;         } else {
;             XB_SPIN(xb_ld(&bar[XB_XGEN(b.x)]) == gen, bar);
;             __builtin_amdgcn_fence(__ATOMIC_ACQUIRE, "agent");
;             asm volatile("s_waitcnt vmcnt(0)" ::: "memory");
;         }
;     }
;     __syncthreads();
; }
.LBB0_186:
	s_load_dwordx2 s[16:17], s[96:97], 0xa0
	s_lshl_b32 s6, s0, 2
	s_add_u32 s6, s10, s6
	s_addc_u32 s7, s11, 0
	s_add_u32 s6, s6, 0x1400
	s_addc_u32 s7, s7, 0
	v_mov_b32_e32 v1, 0
	v_mov_b32_e32 v3, 1
	v_mov_b32_e32 v4, 1
	s_waitcnt lgkmcnt(0)
	v_readfirstlane_b32 s8, v2
	v_readfirstlane_b32 s9, v0
	global_atomic_add v4, v1, v4, s[6:7] sc0
	s_add_u32 s12, s16, 0x7400
	s_addc_u32 s13, s17, 0
	s_add_i32 s98, s98, 1
	s_mul_i32 s8, s98, s8
	s_mul_i32 s9, s98, s9
	s_mov_b32 s14, 0
	s_waitcnt vmcnt(0)
	v_readfirstlane_b32 s6, v4
	s_add_i32 s6, s6, 1
	s_cmp_lg_u32 s6, s8
	s_cbranch_scc1 .Lgb0_poll
	buffer_wbl2 sc1
	s_waitcnt vmcnt(0)
	global_atomic_add v1, v3, s[12:13]
.Lgb0_poll:
	global_load_dword v4, v1, s[12:13] sc1
	s_waitcnt vmcnt(0)
	v_readfirstlane_b32 s6, v4
	s_sub_i32 s6, s6, s9
	s_cmp_ge_i32 s6, 0
	s_cbranch_scc1 .Lgb0_done
	s_sleep 1
	s_add_i32 s14, s14, 1
	s_and_b32 s6, s14, 0xff
	s_cmp_lg_u32 s6, 0
	s_cbranch_scc1 .Lgb0_poll
	global_load_dword v4, v1, s[4:5] sc1
	s_waitcnt vmcnt(0)
	v_readfirstlane_b32 s6, v4
	s_cmp_lg_u32 s6, 0
	s_cbranch_scc1 .Lgb0_done
	s_cmp_lt_u32 s14, 0x40001
	s_cbranch_scc1 .Lgb0_poll
	global_atomic_add v1, v3, s[4:5]
.Lgb0_done:
	s_waitcnt vmcnt(0)
	buffer_inv sc1
	s_waitcnt vmcnt(0)

; __device__ __forceinline__ unsigned xb_ld(unsigned* p)              { return __hip_atomic_load(p, __ATOMIC_RELAXED, __HIP_MEMORY_SCOPE_AGENT); }
; __device__ __forceinline__ unsigned xb_add(unsigned* p, unsigned v) { return __hip_atomic_fetch_add(p, v, __ATOMIC_RELAXED, __HIP_MEMORY_SCOPE_AGENT); }
; #define XB_SPIN(cond, bar) do { unsigned _sp = 0; while (cond) { __builtin_amdgcn_s_sleep(1); \
;     if ((++_sp & 255u) == 0u) { if (xb_ld(&(bar)[XB_TMO])) break; if (_sp > XB_SPIN_CAP) { atomicAdd(&(bar)[XB_TMO], 1u); break; } } } } while (0)
; #define XB_TID() ((int)__builtin_amdgcn_mbcnt_hi(~0u, __builtin_amdgcn_mbcnt_lo(~0u, 0u)) + 64 * xb_wave_id)
; __device__ __forceinline__ void xcd_barrier(const XcdBarrier& b, const int xb_wave_id) {
;     asm volatile("s_waitcnt vmcnt(0)" ::: "memory");
;     __syncthreads();
;     if (XB_TID() == 0) {
;         unsigned* bar = b.bar;
;         __builtin_amdgcn_s_waitcnt(0);
;         unsigned nloc = b.st[0], nx = b.st[1];
;         if (nloc == 0u) { xcd_barrier_complete(bar, b.x, nloc, nx); b.st[0] = nloc; b.st[1] = nx; }
;         const unsigned old = xb_add(&bar[XB_XSUB(b.x)], 1u);
;         const unsigned gen = old / nloc;
;         if (old + 1u == (gen + 1u) * nloc) {
;             __builtin_amdgcn_fence(__ATOMIC_RELEASE, "agent");
;             asm volatile("s_waitcnt vmcnt(0)" ::: "memory");
;             const unsigned og = xb_add(&bar[XB_TOP], 1u);
;             const unsigned tg = og / nx;
;             if (og + 1u == (tg + 1u) * nx) xb_add(&bar[XB_TOPGEN], 1u);
;             else XB_SPIN(xb_ld(&bar[XB_TOPGEN]) == tg, bar);
;             __builtin_amdgcn_fence(__ATOMIC_ACQUIRE, "agent");
;             xb_add(&bar[XB_XGEN(b.x)], 1u);
;             asm volatile("s_waitcnt vmcnt(0)" ::: "memory");
;         } else {
;             XB_SPIN(xb_ld(&bar[XB_XGEN(b.x)]) == gen, bar);
;             __builtin_amdgcn_fence(__ATOMIC_ACQUIRE, "agent");
;             asm volatile("s_waitcnt vmcnt(0)" ::: "memory");
;         }
;     }
;     __syncthreads();
; }
.LBB0_257:
	v_readlane_b32 s2, v251, 41
	v_readlane_b32 s3, v251, 42
	v_mov_b32_e32 v4, 1
	v_mov_b32_e32 v5, 1
	s_waitcnt lgkmcnt(0)
	v_readfirstlane_b32 s4, v3
	v_readfirstlane_b32 s5, v2
	s_nop 1
	global_atomic_add v4, v1, v4, s[2:3] sc0
	s_add_i32 s98, s98, 1
	s_mul_i32 s8, s98, s4
	s_mul_i32 s9, s98, s5
	v_readlane_b32 s12, v251, 45
	v_readlane_b32 s13, v251, 46
	s_mov_b32 s14, 0
	s_waitcnt vmcnt(0)
	v_readfirstlane_b32 s2, v4
	s_add_i32 s2, s2, 1
	s_cmp_lg_u32 s2, s8
	s_cbranch_scc1 .Lgb1_poll
	buffer_wbl2 sc1
	s_waitcnt vmcnt(0)
	global_atomic_add v1, v5, s[12:13]
.Lgb1_poll:
	global_load_dword v4, v1, s[12:13] sc1
	s_waitcnt vmcnt(0)
	v_readfirstlane_b32 s2, v4
	s_sub_i32 s2, s2, s9
	s_cmp_ge_i32 s2, 0
	s_cbranch_scc1 .Lgb1_done
	s_sleep 1
	s_add_i32 s14, s14, 1
	s_and_b32 s2, s14, 0xff
	s_cmp_lg_u32 s2, 0
	s_cbranch_scc1 .Lgb1_poll
	global_load_dword v4, v1, s[48:49] sc1
	s_waitcnt vmcnt(0)
	v_readfirstlane_b32 s2, v4
	s_cmp_lg_u32 s2, 0
	s_cbranch_scc1 .Lgb1_done
	s_cmp_lt_u32 s14, 0x40001
	s_cbranch_scc1 .Lgb1_poll
	global_atomic_add v1, v5, s[48:49]

; __device__ __forceinline__ unsigned xb_ld(unsigned* p)              { return __hip_atomic_load(p, __ATOMIC_RELAXED, __HIP_MEMORY_SCOPE_AGENT); }
; __device__ __forceinline__ unsigned xb_add(unsigned* p, unsigned v) { return __hip_atomic_fetch_add(p, v, __ATOMIC_RELAXED, __HIP_MEMORY_SCOPE_AGENT); }
; #define XB_SPIN(cond, bar) do { unsigned _sp = 0; while (cond) { __builtin_amdgcn_s_sleep(1); \
;     if ((++_sp & 255u) == 0u) { if (xb_ld(&(bar)[XB_TMO])) break; if (_sp > XB_SPIN_CAP) { atomicAdd(&(bar)[XB_TMO], 1u); break; } } } } while (0)
; #define XB_TID() ((int)__builtin_amdgcn_mbcnt_hi(~0u, __builtin_amdgcn_mbcnt_lo(~0u, 0u)) + 64 * xb_wave_id)
; __device__ __forceinline__ void xcd_barrier(const XcdBarrier& b, const int xb_wave_id) {
;     asm volatile("s_waitcnt vmcnt(0)" ::: "memory");
;     __syncthreads();
;     if (XB_TID() == 0) {
;         unsigned* bar = b.bar;
;         __builtin_amdgcn_s_waitcnt(0);
;         unsigned nloc = b.st[0], nx = b.st[1];
;         if (nloc == 0u) { xcd_barrier_complete(bar, b.x, nloc, nx); b.st[0] = nloc; b.st[1] = nx; }
;         const unsigned old = xb_add(&bar[XB_XSUB(b.x)], 1u);
;         const unsigned gen = old / nloc;
;         if (old + 1u == (gen + 1u) * nloc) {
;             __builtin_amdgcn_fence(__ATOMIC_RELEASE, "agent");
;             asm volatile("s_waitcnt vmcnt(0)" ::: "memory");
;             const unsigned og = xb_add(&bar[XB_TOP], 1u);
;             const unsigned tg = og / nx;
;             if (og + 1u == (tg + 1u) * nx) xb_add(&bar[XB_TOPGEN], 1u);
;             else XB_SPIN(xb_ld(&bar[XB_TOPGEN]) == tg, bar);
;             __builtin_amdgcn_fence(__ATOMIC_ACQUIRE, "agent");
;             xb_add(&bar[XB_XGEN(b.x)], 1u);
;             asm volatile("s_waitcnt vmcnt(0)" ::: "memory");
;         } else {
;             XB_SPIN(xb_ld(&bar[XB_XGEN(b.x)]) == gen, bar);
;             __builtin_amdgcn_fence(__ATOMIC_ACQUIRE, "agent");
;             asm volatile("s_waitcnt vmcnt(0)" ::: "memory");
;         }
;     }
;     __syncthreads();
; }
.Lgb5_done:
	s_waitcnt vmcnt(0)
	buffer_inv sc1
	s_waitcnt vmcnt(0)
	s_branch .LBB0_225

; __global__ void __launch_bounds__(NWAVES * 64, 2) trunk_fwd(Args a) {
;     extern __shared__ __attribute__((aligned(16))) unsigned char lds_raw[];
	.amdhsa_kernel _Z9trunk_fwd4Args
		.amdhsa_group_segment_fixed_size 0
		.amdhsa_private_segment_fixed_size 0
		.amdhsa_kernarg_size 432
		.amdhsa_user_sgpr_count 2
		.amdhsa_user_sgpr_dispatch_ptr 0
		.amdhsa_user_sgpr_queue_ptr 0
		.amdhsa_user_sgpr_kernarg_segment_ptr 1
		.amdhsa_user_sgpr_dispatch_id 0
		.amdhsa_user_sgpr_kernarg_preload_length 0
		.amdhsa_user_sgpr_kernarg_preload_offset 0
		.amdhsa_user_sgpr_private_segment_size 0
		.amdhsa_uses_dynamic_stack 0
		.amdhsa_enable_private_segment 0
		.amdhsa_system_sgpr_workgroup_id_x 1
		.amdhsa_system_sgpr_workgroup_id_y 0
		.amdhsa_system_sgpr_workgroup_id_z 0
		.amdhsa_system_sgpr_workgroup_info 0
		.amdhsa_system_vgpr_workitem_id 0
		.amdhsa_next_free_vgpr 253
		.amdhsa_next_free_sgpr 100
		.amdhsa_accum_offset 256
		.amdhsa_reserve_vcc 1
		.amdhsa_float_round_mode_32 0
		.amdhsa_float_round_mode_16_64 0
		.amdhsa_float_denorm_mode_32 3
		.amdhsa_float_denorm_mode_16_64 3
		.amdhsa_dx10_clamp 1
		.amdhsa_ieee_mode 1
		.amdhsa_fp16_overflow 0
		.amdhsa_tg_split 0
		.amdhsa_exception_fp_ieee_invalid_op 0
		.amdhsa_exception_fp_denorm_src 0
		.amdhsa_exception_fp_ieee_div_zero 0
		.amdhsa_exception_fp_ieee_overflow 0
		.amdhsa_exception_fp_ieee_underflow 0
		.amdhsa_exception_fp_ieee_inexact 0
		.amdhsa_exception_int_div_zero 0
	.end_amdhsa_kernel

; __global__ void __launch_bounds__(NWAVES * 64, 2) trunk_fwd(Args a) {
;     extern __shared__ __attribute__((aligned(16))) unsigned char lds_raw[];
amdhsa.kernels:
  - .agpr_count:     0
    .args:
      - .offset:         0
        .size:           176
        .value_kind:     by_value
      - .offset:         176
        .size:           4
        .value_kind:     hidden_block_count_x
      - .offset:         180
        .size:           4
        .value_kind:     hidden_block_count_y
      - .offset:         184
        .size:           4
        .value_kind:     hidden_block_count_z
      - .offset:         188
        .size:           2
        .value_kind:     hidden_group_size_x
      - .offset:         190
        .size:           2
        .value_kind:     hidden_group_size_y
      - .offset:         192
        .size:           2
        .value_kind:     hidden_group_size_z
      - .offset:         194
        .size:           2
        .value_kind:     hidden_remainder_x
      - .offset:         196
        .size:           2
        .value_kind:     hidden_remainder_y
      - .offset:         198
        .size:           2
        .value_kind:     hidden_remainder_z
      - .offset:         216
        .size:           8
        .value_kind:     hidden_global_offset_x
      - .offset:         224
        .size:           8
        .value_kind:     hidden_global_offset_y
      - .offset:         232
        .size:           8
        .value_kind:     hidden_global_offset_z
      - .offset:         240
        .size:           2
        .value_kind:     hidden_grid_dims
      - .offset:         296
        .size:           4
        .value_kind:     hidden_dynamic_lds_size
    .group_segment_fixed_size: 0
    .kernarg_segment_align: 8
    .kernarg_segment_size: 432
    .language:       OpenCL C
    .language_version:
      - 2
      - 0
    .max_flat_workgroup_size: 512
    .name:           _Z9trunk_fwd4Args
    .private_segment_fixed_size: 0
    .sgpr_count:     106
    .sgpr_spill_count: 385
    .symbol:         _Z9trunk_fwd4Args.kd
    .uniform_work_group_size: 1
    .uses_dynamic_stack: false
    .vgpr_count:     253
    .vgpr_spill_count: 0
    .wavefront_size: 64
